# v24: v21 + grid barrier: non-last workgroups poll the top generation word directly (one release hop less)
# baseline (speedup 1.0000x reference)
.LBB0_274:
	s_or_b64 exec, exec, s[4:5]
	v_cvt_f32_u32_e32 v5, v3
	s_waitcnt vmcnt(0)
	v_readfirstlane_b32 s0, v4
	v_sub_u32_e32 v4, 0, v3
	v_rcp_iflag_f32_e32 v5, v5
	v_add_u32_e32 v6, s0, v1
	v_mul_f32_e32 v5, 0x4f7ffffe, v5
	v_cvt_u32_f32_e32 v5, v5
	v_mul_lo_u32 v1, v4, v5
	v_mul_hi_u32 v1, v5, v1
	v_add_u32_e32 v1, v5, v1
	v_mul_hi_u32 v1, v6, v1
	v_mul_lo_u32 v4, v1, v3
	v_sub_u32_e32 v4, v6, v4
	v_add_u32_e32 v5, 1, v1
	v_cmp_ge_u32_e32 vcc, v4, v3
	s_nop 1
	v_cndmask_b32_e32 v1, v1, v5, vcc
	v_sub_u32_e32 v5, v4, v3
	v_cndmask_b32_e32 v4, v4, v5, vcc
	v_add_u32_e32 v5, 1, v1
	v_cmp_ge_u32_e32 vcc, v4, v3
	v_add_u32_e32 v4, 1, v6
	s_nop 0
	v_cndmask_b32_e32 v1, v1, v5, vcc
	v_mul_lo_u32 v5, v3, v1
	v_add_u32_e32 v3, v5, v3
	v_cmp_ne_u32_e32 vcc, v4, v3
	s_and_saveexec_b64 s[0:1], vcc
	s_xor_b64 s[4:5], exec, s[0:1]
	s_cbranch_execz .LBB0_288
	s_getreg_b32 s0, hwreg(HW_REG_XCC_ID, 0, 4)
	s_lshl_b32 s0, s0, 8
	s_sub_u32 s0, 0x1100, s0
	v_mov_b32_e32 v5, s0
	v_readlane_b32 s0, v251, 17
	v_readlane_b32 s1, v251, 18
	s_waitcnt lgkmcnt(0)
	s_nop 3
	global_load_dword v2, v5, s[0:1] sc1
	s_waitcnt vmcnt(0)
	v_cmp_eq_u32_e32 vcc, v2, v1
	s_and_saveexec_b64 s[6:7], vcc
	s_cbranch_execz .LBB0_287
	s_mov_b32 s0, 1
	s_mov_b64 s[8:9], 0
	s_branch .LBB0_278

.LBB0_282:
	v_readlane_b32 s12, v251, 17
	v_readlane_b32 s13, v251, 18
	s_add_i32 s0, s0, 1
	s_mov_b64 s[22:23], -1
	s_nop 2
	global_load_dword v2, v5, s[12:13] sc1
	s_waitcnt vmcnt(0)
	v_cmp_ne_u32_e32 vcc, v2, v1
	s_orn2_b64 s[12:13], vcc, exec
	s_branch .LBB0_277

.LBB0_402:
	s_or_b64 exec, exec, s[4:5]
	v_cvt_f32_u32_e32 v5, v3
	s_waitcnt vmcnt(0)
	v_readfirstlane_b32 s1, v4
	v_sub_u32_e32 v4, 0, v3
	v_rcp_iflag_f32_e32 v5, v5
	v_add_u32_e32 v6, s1, v1
	v_mul_f32_e32 v5, 0x4f7ffffe, v5
	v_cvt_u32_f32_e32 v5, v5
	v_mul_lo_u32 v1, v4, v5
	v_mul_hi_u32 v1, v5, v1
	v_add_u32_e32 v1, v5, v1
	v_mul_hi_u32 v1, v6, v1
	v_mul_lo_u32 v4, v1, v3
	v_sub_u32_e32 v4, v6, v4
	v_add_u32_e32 v5, 1, v1
	v_cmp_ge_u32_e32 vcc, v4, v3
	s_nop 1
	v_cndmask_b32_e32 v1, v1, v5, vcc
	v_sub_u32_e32 v5, v4, v3
	v_cndmask_b32_e32 v4, v4, v5, vcc
	v_add_u32_e32 v5, 1, v1
	v_cmp_ge_u32_e32 vcc, v4, v3
	v_add_u32_e32 v4, 1, v6
	s_nop 0
	v_cndmask_b32_e32 v1, v1, v5, vcc
	v_mul_lo_u32 v5, v3, v1
	v_add_u32_e32 v3, v5, v3
	v_cmp_ne_u32_e32 vcc, v4, v3
	s_and_saveexec_b64 s[4:5], vcc
	s_xor_b64 s[4:5], exec, s[4:5]
	s_cbranch_execz .LBB0_416
	s_getreg_b32 s6, hwreg(HW_REG_XCC_ID, 0, 4)
	s_lshl_b32 s6, s6, 8
	s_sub_u32 s6, 0x1100, s6
	v_mov_b32_e32 v5, s6
	v_readlane_b32 s6, v251, 17
	v_readlane_b32 s7, v251, 18
	s_waitcnt lgkmcnt(0)
	s_nop 3
	global_load_dword v2, v5, s[6:7] sc1
	s_waitcnt vmcnt(0)
	v_cmp_eq_u32_e32 vcc, v2, v1
	s_and_saveexec_b64 s[6:7], vcc
	s_cbranch_execz .LBB0_415
	s_mov_b32 s1, 1
	s_mov_b64 s[8:9], 0
	s_branch .LBB0_406

.LBB0_410:
	v_readlane_b32 s12, v251, 17
	v_readlane_b32 s13, v251, 18
	s_add_i32 s1, s1, 1
	s_mov_b64 s[22:23], -1
	s_nop 2
	global_load_dword v2, v5, s[12:13] sc1
	s_waitcnt vmcnt(0)
	v_cmp_ne_u32_e32 vcc, v2, v1
	s_orn2_b64 s[12:13], vcc, exec
	s_branch .LBB0_405

.LBB0_512:
	s_or_b64 exec, exec, s[4:5]
	v_cvt_f32_u32_e32 v5, v3
	s_waitcnt vmcnt(0)
	v_readfirstlane_b32 s0, v4
	v_sub_u32_e32 v4, 0, v3
	v_rcp_iflag_f32_e32 v5, v5
	v_add_u32_e32 v6, s0, v1
	v_mul_f32_e32 v5, 0x4f7ffffe, v5
	v_cvt_u32_f32_e32 v5, v5
	v_mul_lo_u32 v1, v4, v5
	v_mul_hi_u32 v1, v5, v1
	v_add_u32_e32 v1, v5, v1
	v_mul_hi_u32 v1, v6, v1
	v_mul_lo_u32 v4, v1, v3
	v_sub_u32_e32 v4, v6, v4
	v_add_u32_e32 v5, 1, v1
	v_cmp_ge_u32_e32 vcc, v4, v3
	s_nop 1
	v_cndmask_b32_e32 v1, v1, v5, vcc
	v_sub_u32_e32 v5, v4, v3
	v_cndmask_b32_e32 v4, v4, v5, vcc
	v_add_u32_e32 v5, 1, v1
	v_cmp_ge_u32_e32 vcc, v4, v3
	v_add_u32_e32 v4, 1, v6
	s_nop 0
	v_cndmask_b32_e32 v1, v1, v5, vcc
	v_mul_lo_u32 v5, v3, v1
	v_add_u32_e32 v3, v5, v3
	v_cmp_ne_u32_e32 vcc, v4, v3
	s_and_saveexec_b64 s[0:1], vcc
	s_xor_b64 s[4:5], exec, s[0:1]
	s_cbranch_execz .LBB0_526
	s_getreg_b32 s0, hwreg(HW_REG_XCC_ID, 0, 4)
	s_lshl_b32 s0, s0, 8
	s_sub_u32 s0, 0x1100, s0
	v_mov_b32_e32 v5, s0
	v_readlane_b32 s0, v251, 17
	v_readlane_b32 s1, v251, 18
	s_waitcnt lgkmcnt(0)
	s_nop 3
	global_load_dword v2, v5, s[0:1] sc1
	s_waitcnt vmcnt(0)
	v_cmp_eq_u32_e32 vcc, v2, v1
	s_and_saveexec_b64 s[6:7], vcc
	s_cbranch_execz .LBB0_525
	s_mov_b32 s0, 1
	s_mov_b64 s[10:11], 0
	s_branch .LBB0_516

.LBB0_520:
	v_readlane_b32 s16, v251, 17
	v_readlane_b32 s17, v251, 18
	s_add_i32 s0, s0, 1
	s_mov_b64 s[26:27], -1
	s_nop 2
	global_load_dword v2, v5, s[16:17] sc1
	s_waitcnt vmcnt(0)
	v_cmp_ne_u32_e32 vcc, v2, v1
	s_orn2_b64 s[22:23], vcc, exec
	s_branch .LBB0_515

.LBB0_742:
	s_or_b64 exec, exec, s[4:5]
	v_cvt_f32_u32_e32 v5, v3
	s_waitcnt vmcnt(0)
	v_readfirstlane_b32 s1, v4
	v_sub_u32_e32 v4, 0, v3
	v_rcp_iflag_f32_e32 v5, v5
	v_add_u32_e32 v6, s1, v1
	v_mul_f32_e32 v5, 0x4f7ffffe, v5
	v_cvt_u32_f32_e32 v5, v5
	v_mul_lo_u32 v1, v4, v5
	v_mul_hi_u32 v1, v5, v1
	v_add_u32_e32 v1, v5, v1
	v_mul_hi_u32 v1, v6, v1
	v_mul_lo_u32 v4, v1, v3
	v_sub_u32_e32 v4, v6, v4
	v_add_u32_e32 v5, 1, v1
	v_cmp_ge_u32_e32 vcc, v4, v3
	s_nop 1
	v_cndmask_b32_e32 v1, v1, v5, vcc
	v_sub_u32_e32 v5, v4, v3
	v_cndmask_b32_e32 v4, v4, v5, vcc
	v_add_u32_e32 v5, 1, v1
	v_cmp_ge_u32_e32 vcc, v4, v3
	v_add_u32_e32 v4, 1, v6
	s_nop 0
	v_cndmask_b32_e32 v1, v1, v5, vcc
	v_mul_lo_u32 v5, v3, v1
	v_add_u32_e32 v3, v5, v3
	v_cmp_ne_u32_e32 vcc, v4, v3
	s_and_saveexec_b64 s[4:5], vcc
	s_xor_b64 s[4:5], exec, s[4:5]
	s_cbranch_execz .LBB0_756
	s_getreg_b32 s8, hwreg(HW_REG_XCC_ID, 0, 4)
	s_lshl_b32 s8, s8, 8
	s_sub_u32 s8, 0x1100, s8
	v_mov_b32_e32 v5, s8
	v_readlane_b32 s8, v251, 17
	v_readlane_b32 s9, v251, 18
	s_waitcnt lgkmcnt(0)
	s_nop 3
	global_load_dword v2, v5, s[8:9] sc1
	s_waitcnt vmcnt(0)
	v_cmp_eq_u32_e32 vcc, v2, v1
	s_and_saveexec_b64 s[8:9], vcc
	s_cbranch_execz .LBB0_755
	s_mov_b32 s1, 1
	s_mov_b64 s[10:11], 0
	s_branch .LBB0_746

.LBB0_750:
	v_readlane_b32 s16, v251, 17
	v_readlane_b32 s17, v251, 18
	s_add_i32 s1, s1, 1
	s_mov_b64 s[26:27], -1
	s_nop 2
	global_load_dword v2, v5, s[16:17] sc1
	s_waitcnt vmcnt(0)
	v_cmp_ne_u32_e32 vcc, v2, v1
	s_orn2_b64 s[22:23], vcc, exec
	s_branch .LBB0_745

.LBB0_1755:
	s_or_b64 exec, exec, s[8:9]
	v_cvt_f32_u32_e32 v5, v3
	s_waitcnt vmcnt(0)
	v_readfirstlane_b32 s0, v4
	v_sub_u32_e32 v4, 0, v3
	v_rcp_iflag_f32_e32 v5, v5
	v_add_u32_e32 v6, s0, v1
	v_mul_f32_e32 v5, 0x4f7ffffe, v5
	v_cvt_u32_f32_e32 v5, v5
	v_mul_lo_u32 v1, v4, v5
	v_mul_hi_u32 v1, v5, v1
	v_add_u32_e32 v1, v5, v1
	v_mul_hi_u32 v1, v6, v1
	v_mul_lo_u32 v4, v1, v3
	v_sub_u32_e32 v4, v6, v4
	v_add_u32_e32 v5, 1, v1
	v_cmp_ge_u32_e32 vcc, v4, v3
	s_nop 1
	v_cndmask_b32_e32 v1, v1, v5, vcc
	v_sub_u32_e32 v5, v4, v3
	v_cndmask_b32_e32 v4, v4, v5, vcc
	v_add_u32_e32 v5, 1, v1
	v_cmp_ge_u32_e32 vcc, v4, v3
	v_add_u32_e32 v4, 1, v6
	s_nop 0
	v_cndmask_b32_e32 v1, v1, v5, vcc
	v_mul_lo_u32 v5, v3, v1
	v_add_u32_e32 v3, v5, v3
	v_cmp_ne_u32_e32 vcc, v4, v3
	s_and_saveexec_b64 s[0:1], vcc
	s_xor_b64 s[8:9], exec, s[0:1]
	s_cbranch_execz .LBB0_1769
	s_getreg_b32 s0, hwreg(HW_REG_XCC_ID, 0, 4)
	s_lshl_b32 s0, s0, 8
	s_sub_u32 s0, 0x1100, s0
	v_mov_b32_e32 v5, s0
	v_readlane_b32 s0, v251, 17
	v_readlane_b32 s1, v251, 18
	s_waitcnt lgkmcnt(0)
	s_nop 3
	global_load_dword v2, v5, s[0:1] sc1
	s_waitcnt vmcnt(0)
	v_cmp_eq_u32_e32 vcc, v2, v1
	s_and_saveexec_b64 s[12:13], vcc
	s_cbranch_execz .LBB0_1768
	s_mov_b32 s0, 1
	s_mov_b64 s[22:23], 0
	s_branch .LBB0_1759

.LBB0_1763:
	v_readlane_b32 s16, v251, 17
	v_readlane_b32 s17, v251, 18
	s_add_i32 s0, s0, 1
	s_mov_b64 s[44:45], -1
	s_nop 2
	global_load_dword v2, v5, s[16:17] sc1
	s_waitcnt vmcnt(0)
	v_cmp_ne_u32_e32 vcc, v2, v1
	s_orn2_b64 s[42:43], vcc, exec
	s_branch .LBB0_1758
